# v63 + dropped the compiler's s_waitcnt vmcnt(0) at the entry of each attention unit (only weight-copy store acknowledgements were outstanding there)
# baseline (speedup 1.0000x reference)
.LBB6_1210:
	s_and_b32 s0, s84, 8
	s_or_b32 s0, s0, s59
	s_sub_i32 s37, 7, s92
	s_lshr_b32 s36, s0, 2
	s_mov_b64 s[6:7], -1
	s_mov_b64 s[2:3], 0
	s_cmp_lt_i32 s93, 1
	s_mov_b64 s[4:5], 0
	s_cbranch_scc1 .LBB6_1224
	s_cmp_gt_i32 s93, 1
	s_cbranch_scc0 .LBB6_1252
	s_cmp_eq_u32 s93, 2
	s_mov_b64 s[4:5], -1
	s_cbranch_scc0 .LBB6_1251
	s_lshl_b32 s1, s37, 8
	s_lshl_b32 s6, s36, 11
	v_readlane_b32 s4, v254, 13
	s_add_i32 s0, s1, 0x100
	s_add_i32 s26, s1, s6
	v_readlane_b32 s5, v254, 14
	s_lshr_b32 s0, s0, 6
	s_mul_i32 s7, s26, 0x600
	s_mul_hi_u32 s6, s26, 0x600
	s_add_u32 s7, s4, s7
	s_addc_u32 s6, s5, s6
	s_add_u32 s7, s7, s71
	s_addc_u32 s6, s6, 0
	s_add_u32 s12, s7, 0x7200000
	s_addc_u32 s13, s6, 0
	s_mul_i32 s6, s36, 0x300000
	s_add_u32 s6, s4, s6
	s_addc_u32 s7, s5, 0
	s_add_u32 s6, s6, s71
	s_addc_u32 s7, s7, 0
	s_add_u32 s6, s6, 0x7e00000
	s_addc_u32 s7, s7, 0
	s_add_u32 s24, s4, s75
	s_addc_u32 s25, s5, 0
	s_lshl_b32 s27, s36, 12
	s_add_u32 s24, s24, s27
	v_mov_b32_e32 v183, v0
	s_addc_u32 s25, s25, 0
	v_mov_b32_e32 v34, v0
	s_add_u32 s24, s24, 0xf300000
	s_addc_u32 s25, s25, 0
	v_readfirstlane_b32 s27, v34
	s_ashr_i32 s27, s27, 1
	s_movk_i32 s28, 0xffe0
	v_mov_b32_e32 v2, s27
	v_bfi_b32 v2, s28, v2, v34
	v_mov_b64_e32 v[4:5], s[12:13]
	v_bfe_u32 v35, v34, 5, 1
	v_mad_i64_i32 v[4:5], s[12:13], v2, s70, v[4:5]
	v_lshlrev_b32_e32 v2, 4, v35
	s_mov_b32 s12, 0x2aaaaaab
	v_lshl_add_u64 v[24:25], v[4:5], 0, v[2:3]
	v_mul_hi_i32 v4, v34, s12
	v_lshrrev_b32_e32 v5, 31, v4
	v_ashrrev_i32_e32 v4, 2, v4
	v_add_u32_e32 v189, v4, v5
	v_mul_lo_u32 v4, v189, 24
	v_sub_u32_e32 v36, v34, v4
	v_add_u32_e32 v4, 0x200, v34
	v_mul_hi_i32 v5, v4, s12
	v_lshrrev_b32_e32 v6, 31, v5
	v_ashrrev_i32_e32 v5, 2, v5
	v_add_u32_e32 v190, v5, v6
	v_mul_lo_u32 v5, v190, 24
	v_sub_u32_e32 v37, v4, v5
	v_add_u32_e32 v4, 0x400, v34
	v_mul_hi_i32 v5, v4, s12
	v_lshrrev_b32_e32 v6, 31, v5
	v_ashrrev_i32_e32 v5, 2, v5
	v_add_u32_e32 v192, v5, v6
	v_mul_lo_u32 v5, v192, 24
	v_sub_u32_e32 v38, v4, v5
	v_lshlrev_b32_e32 v14, 3, v38
	v_ashrrev_i32_e32 v15, 31, v14
	v_lshlrev_b32_e32 v6, 3, v36
	v_lshlrev_b32_e32 v8, 3, v37
	v_lshlrev_b64 v[32:33], 1, v[14:15]
	v_lshlrev_b32_e32 v14, 4, v34
	v_ashrrev_i32_e32 v39, 3, v34
	v_mov_b64_e32 v[26:27], s[6:7]
	v_ashrrev_i32_e32 v7, 31, v6
	v_ashrrev_i32_e32 v9, 31, v8
	v_and_b32_e32 v168, 0x70, v14
	v_mov_b32_e32 v169, v3
	v_mad_i64_i32 v[4:5], s[12:13], v189, s70, v[26:27]
	v_lshlrev_b64 v[28:29], 1, v[6:7]
	v_mad_i64_i32 v[6:7], s[12:13], v190, s70, v[26:27]
	v_lshlrev_b64 v[30:31], 1, v[8:9]
	v_mad_i64_i32 v[12:13], s[12:13], v192, s70, v[26:27]
	v_lshl_add_u64 v[170:171], s[24:25], 0, v[168:169]
	v_add_u32_e32 v40, 64, v39
	v_lshl_add_u64 v[4:5], v[4:5], 0, v[28:29]
	v_lshl_add_u64 v[8:9], v[6:7], 0, v[30:31]
	v_lshl_add_u64 v[12:13], v[12:13], 0, v[32:33]
	v_mad_i64_i32 v[16:17], s[12:13], v39, s55, v[170:171]
	v_mad_i64_i32 v[20:21], s[12:13], v40, s55, v[170:171]
	global_load_dwordx4 v[4:7], v[4:5], off
	s_nop 0
	global_load_dwordx4 v[8:11], v[8:9], off
	s_nop 0
	global_load_dwordx4 v[12:15], v[12:13], off
	s_nop 0
	global_load_dwordx4 v[16:19], v[16:17], off
	s_nop 0
	global_load_dwordx4 v[20:23], v[20:21], off
	s_nop 0
	global_load_dwordx4 v[144:147], v[24:25], off
	global_load_dwordx4 v[140:143], v[24:25], off offset:32
	global_load_dwordx4 v[136:139], v[24:25], off offset:64
	global_load_dwordx4 v[132:135], v[24:25], off offset:96
	global_load_dwordx4 v[128:131], v[24:25], off offset:128
	global_load_dwordx4 v[124:127], v[24:25], off offset:160
	global_load_dwordx4 v[120:123], v[24:25], off offset:192
	global_load_dwordx4 v[116:119], v[24:25], off offset:224
	global_load_dwordx4 v[112:115], v[24:25], off offset:256
	global_load_dwordx4 v[108:111], v[24:25], off offset:288
	global_load_dwordx4 v[104:107], v[24:25], off offset:320
	global_load_dwordx4 v[100:103], v[24:25], off offset:352
	v_add_u32_e32 v24, 64, v189
	v_mad_i64_i32 v[24:25], s[12:13], v24, s70, v[26:27]
	v_lshl_add_u64 v[24:25], v[24:25], 0, v[28:29]
	global_load_dwordx4 v[148:151], v[24:25], off
	v_add_u32_e32 v24, 64, v190
	v_mad_i64_i32 v[24:25], s[12:13], v24, s70, v[26:27]
	v_add_u32_e32 v41, 64, v192
	v_lshl_add_u64 v[24:25], v[24:25], 0, v[30:31]
	v_mad_i64_i32 v[26:27], s[12:13], v41, s70, v[26:27]
	v_lshl_add_u64 v[26:27], v[26:27], 0, v[32:33]
	global_load_dwordx4 v[152:155], v[24:25], off
	global_load_dwordx4 v[156:159], v[26:27], off
	v_mov_b64_e32 v[24:25], s[24:25]
	v_mad_i64_i32 v[26:27], s[12:13], v39, s55, v[24:25]
	v_lshl_add_u64 v[26:27], v[26:27], 0, v[168:169]
	v_mad_i64_i32 v[24:25], s[12:13], v40, s55, v[24:25]
	v_lshl_add_u64 v[24:25], v[24:25], 0, v[168:169]
	global_load_dwordx4 v[160:163], v[26:27], off offset:128
	global_load_dwordx4 v[164:167], v[24:25], off offset:128
	s_and_b32 s25, s27, 0xffffffe0
	s_add_i32 s12, s25, s1
	v_lshlrev_b32_e32 v24, 1, v34
	v_lshrrev_b32_e32 v25, 1, v34
	s_movk_i32 s1, 0x190
	v_and_b32_e32 v24, 8, v24
	v_and_b32_e32 v25, 4, v25
	v_and_b32_e32 v26, 19, v34
	v_mul_lo_u32 v194, v189, s1
	v_lshlrev_b32_e32 v195, 4, v36
	v_or3_b32 v24, v24, v26, v25
	v_add3_u32 v25, 0, v194, v195
	v_mul_lo_u32 v196, v190, s1
	v_lshlrev_b32_e32 v197, 4, v37
	v_mul_lo_u32 v198, v192, s1
	v_lshlrev_b32_e32 v199, 4, v38
	v_mul_lo_u32 v201, v39, s41
	v_and_b32_e32 v191, 31, v34
	v_mul_i32_i24_e32 v193, -8, v35
	s_lshl_b32 s1, s92, 8
	v_mad_i64_i32 v[172:173], s[28:29], v39, s55, 0
	v_mad_i64_i32 v[174:175], s[28:29], v40, s55, 0
	v_mul_u32_u24_e32 v200, 0x190, v24
	v_lshl_add_u64 v[176:177], s[6:7], 0, v[28:29]
	v_lshl_add_u64 v[178:179], s[6:7], 0, v[30:31]
	v_lshl_add_u64 v[184:185], s[6:7], 0, v[32:33]
	s_mov_b32 s24, 1
	s_or_b32 s13, s12, 31
	v_mul_u32_u24_e32 v169, 0x90, v191
	v_mov_b32_e32 v187, 0
	v_mov_b32_e32 v188, 0xf149f2ca
	s_movk_i32 s84, 0x80
	s_waitcnt vmcnt(21)
	ds_write_b128 v25, v[4:7]
	v_add3_u32 v4, 0, v196, v197
	s_waitcnt vmcnt(20)
	ds_write_b128 v4, v[8:11]
	v_add3_u32 v4, 0, v198, v199
	s_waitcnt vmcnt(19)
	ds_write_b128 v4, v[12:15]
	v_add3_u32 v4, 0, v168, v201
	s_waitcnt vmcnt(18)
	ds_write_b128 v4, v[16:19] offset:25600
	s_waitcnt vmcnt(17)
	ds_write_b128 v4, v[20:23] offset:34816
	v_add3_u32 v4, v193, s25, v191
	v_subrev_u32_e32 v4, s1, v4
	v_mov_b32_e32 v18, v3
	v_mov_b32_e32 v19, v3
	v_add_u32_e32 v202, 0x6e9, v4
	v_mov_b32_e32 v4, v3
	v_mov_b32_e32 v5, v3
	v_mov_b32_e32 v6, v3
	v_mov_b32_e32 v7, v3
	v_mov_b32_e32 v8, v3
	v_mov_b32_e32 v9, v3
	v_mov_b32_e32 v10, v3
	v_mov_b32_e32 v11, v3
	v_mov_b32_e32 v12, v3
	v_mov_b32_e32 v13, v3
	v_mov_b32_e32 v14, v3
	v_mov_b32_e32 v15, v3
	v_mov_b32_e32 v16, v3
	v_mov_b32_e32 v17, v3
	v_mov_b64_e32 v[34:35], v[18:19]
	v_mov_b64_e32 v[50:51], v[18:19]
	v_mov_b64_e32 v[66:67], v[18:19]
	v_mov_b64_e32 v[32:33], v[16:17]
	v_mov_b64_e32 v[30:31], v[14:15]
	v_mov_b64_e32 v[28:29], v[12:13]
	v_mov_b64_e32 v[26:27], v[10:11]
	v_mov_b64_e32 v[24:25], v[8:9]
	v_mov_b64_e32 v[22:23], v[6:7]
	v_mov_b64_e32 v[20:21], v[4:5]
	v_mov_b64_e32 v[48:49], v[16:17]
	v_mov_b64_e32 v[46:47], v[14:15]
	v_mov_b64_e32 v[44:45], v[12:13]
	v_mov_b64_e32 v[42:43], v[10:11]
	v_mov_b64_e32 v[40:41], v[8:9]
	v_mov_b64_e32 v[38:39], v[6:7]
	v_mov_b64_e32 v[36:37], v[4:5]
	v_mov_b64_e32 v[64:65], v[16:17]
	v_mov_b64_e32 v[62:63], v[14:15]
	v_mov_b64_e32 v[60:61], v[12:13]
	v_mov_b64_e32 v[58:59], v[10:11]
	v_mov_b64_e32 v[56:57], v[8:9]
	v_mov_b64_e32 v[54:55], v[6:7]
	v_mov_b64_e32 v[52:53], v[4:5]
	s_waitcnt lgkmcnt(0)
	s_barrier

.LBB6_1226:
	s_and_b64 vcc, exec, s[2:3]
	s_cbranch_vccz .LBB6_1306
	s_lshl_b32 s12, s37, 8
	s_lshl_b32 s0, s36, 11
	s_add_i32 s1, s12, 0x100
	v_readlane_b32 s2, v254, 13
	s_lshr_b32 s13, s1, 6
	s_add_i32 s1, s12, s0
	v_readlane_b32 s3, v254, 14
	s_mul_i32 s5, s1, 0xc00
	s_mul_hi_u32 s4, s1, 0xc00
	s_add_u32 s5, s2, s5
	s_addc_u32 s4, s3, s4
	s_add_u32 s24, s5, 0x8a00000
	s_addc_u32 s25, s4, 0
	s_mul_i32 s36, s36, 0x600000
	s_add_u32 s4, s2, s36
	s_addc_u32 s5, s3, 0
	v_mov_b32_e32 v16, v3
	v_mov_b32_e32 v17, v3
	s_add_u32 s26, s4, 0xa200000
	v_mov_b32_e32 v2, v3
	v_mov_b32_e32 v4, v3
	v_mov_b32_e32 v5, v3
	v_mov_b32_e32 v6, v3
	v_mov_b32_e32 v7, v3
	v_mov_b32_e32 v8, v3
	v_mov_b32_e32 v9, v3
	v_mov_b32_e32 v10, v3
	v_mov_b32_e32 v11, v3
	v_mov_b32_e32 v12, v3
	v_mov_b32_e32 v13, v3
	v_mov_b32_e32 v14, v3
	v_mov_b32_e32 v15, v3
	v_mov_b64_e32 v[66:67], v[16:17]
	v_mov_b64_e32 v[50:51], v[16:17]
	v_mov_b64_e32 v[34:35], v[16:17]
	s_addc_u32 s27, s5, 0
	s_lshl_b32 s4, s92, 8
	v_mov_b64_e32 v[64:65], v[14:15]
	v_mov_b64_e32 v[62:63], v[12:13]
	v_mov_b64_e32 v[60:61], v[10:11]
	v_mov_b64_e32 v[58:59], v[8:9]
	v_mov_b64_e32 v[56:57], v[6:7]
	v_mov_b64_e32 v[54:55], v[4:5]
	v_mov_b64_e32 v[52:53], v[2:3]
	v_mov_b64_e32 v[48:49], v[14:15]
	v_mov_b64_e32 v[46:47], v[12:13]
	v_mov_b64_e32 v[44:45], v[10:11]
	v_mov_b64_e32 v[42:43], v[8:9]
	v_mov_b64_e32 v[40:41], v[6:7]
	v_mov_b64_e32 v[38:39], v[4:5]
	v_mov_b64_e32 v[36:37], v[2:3]
	v_mov_b64_e32 v[32:33], v[14:15]
	v_mov_b64_e32 v[30:31], v[12:13]
	v_mov_b64_e32 v[28:29], v[10:11]
	v_mov_b64_e32 v[26:27], v[8:9]
	v_mov_b64_e32 v[24:25], v[6:7]
	v_mov_b64_e32 v[22:23], v[4:5]
	v_mov_b64_e32 v[20:21], v[2:3]
	v_mov_b64_e32 v[18:19], v[16:17]
	v_mov_b32_e32 v183, v0
	s_sub_i32 s28, 0x71f, s4
	s_mov_b32 s29, 0
	v_mov_b32_e32 v229, 0xf149f2ca
	v_mov_b32_e32 v230, 0
	s_lshl_b32 s30, s0, 1
	v_mov_b64_e32 v[16:17], v[14:15]
	v_mov_b64_e32 v[14:15], v[12:13]
	v_mov_b64_e32 v[12:13], v[10:11]
	v_mov_b64_e32 v[10:11], v[8:9]
	v_mov_b64_e32 v[8:9], v[6:7]
	v_mov_b64_e32 v[6:7], v[4:5]
	v_mov_b64_e32 v[4:5], v[2:3]
	s_branch .LBB6_1229

.LBB6_1252:
	s_and_b64 vcc, exec, s[6:7]
	s_cbranch_vccz .LBB6_1288
	s_lshl_b32 s48, s37, 8
	s_lshl_b32 s0, s36, 11
	v_readlane_b32 s28, v254, 13
	s_add_i32 s1, s48, 0x100
	s_add_i32 s34, s48, s0
	s_mov_b32 s35, s85
	v_readlane_b32 s29, v254, 14
	s_lshr_b32 s47, s1, 6
	s_lshl_b64 s[0:1], s[34:35], 10
	s_add_u32 s0, s28, s0
	s_addc_u32 s1, s29, s1
	s_lshl_b32 s30, s74, 1
	s_add_u32 s0, s0, s30
	s_addc_u32 s1, s1, 0
	s_add_u32 s24, s0, 0x6200000
	s_addc_u32 s25, s1, 0
	s_lshl_b32 s0, s36, 21
	s_add_u32 s0, s28, s0
	s_addc_u32 s1, s29, 0
	s_add_u32 s0, s0, s30
	s_addc_u32 s1, s1, 0
	s_add_u32 s26, s0, 0x6a00000
	v_mov_b32_e32 v145, v0
	s_addc_u32 s27, s1, 0
	v_mov_b32_e32 v22, v0
	s_add_u32 s0, s28, s75
	s_addc_u32 s1, s29, 0
	v_ashrrev_i32_e32 v2, 31, v22
	s_lshl_b32 s6, s36, 12
	v_lshrrev_b32_e32 v2, 29, v2
	s_add_u32 s0, s0, s6
	v_add_u32_e32 v2, v22, v2
	s_addc_u32 s1, s1, 0
	v_ashrrev_i32_e32 v128, 3, v2
	v_and_b32_e32 v2, -8, v2
	s_add_u32 s6, s0, 0xca00000
	v_sub_u32_e32 v24, v22, v2
	v_lshlrev_b32_e32 v2, 4, v22
	s_addc_u32 s7, s1, 0
	v_ashrrev_i32_e32 v23, 3, v22
	v_and_b32_e32 v130, 0x70, v2
	v_mov_b32_e32 v131, v3
	v_lshl_add_u64 v[132:133], s[6:7], 0, v[130:131]
	v_add_u32_e32 v25, 64, v23
	v_mad_i64_i32 v[8:9], s[0:1], v23, s55, v[132:133]
	v_mad_i64_i32 v[12:13], s[0:1], v25, s55, v[132:133]
	v_readfirstlane_b32 s0, v22
	s_ashr_i32 s12, s0, 1
	v_ashrrev_i32_e32 v129, 31, v128
	v_lshlrev_b32_e32 v6, 3, v24
	v_mov_b32_e32 v2, s12
	s_movk_i32 s0, 0xffe0
	v_lshlrev_b64 v[4:5], 10, v[128:129]
	v_ashrrev_i32_e32 v7, 31, v6
	v_bfi_b32 v20, s0, v2, v22
	v_lshl_add_u64 v[4:5], s[26:27], 0, v[4:5]
	v_lshlrev_b64 v[16:17], 1, v[6:7]
	v_ashrrev_i32_e32 v21, 31, v20
	v_lshl_add_u64 v[18:19], v[4:5], 0, v[16:17]
	v_bfe_u32 v26, v22, 5, 1
	v_lshlrev_b64 v[20:21], 10, v[20:21]
	s_mov_b32 s0, 0x10000
	global_load_dwordx4 v[4:7], v[18:19], off
	s_nop 0
	global_load_dwordx4 v[8:11], v[8:9], off
	v_lshl_add_u64 v[20:21], s[24:25], 0, v[20:21]
	v_lshlrev_b32_e32 v2, 4, v26
	v_add_co_u32_e32 v18, vcc, s0, v18
	v_lshl_add_u64 v[20:21], v[20:21], 0, v[2:3]
	s_nop 0
	v_addc_co_u32_e32 v19, vcc, 0, v19, vcc
	global_load_dwordx4 v[12:15], v[12:13], off
	s_nop 0
	global_load_dwordx4 v[112:115], v[20:21], off
	global_load_dwordx4 v[108:111], v[20:21], off offset:32
	global_load_dwordx4 v[104:107], v[20:21], off offset:64
	global_load_dwordx4 v[100:103], v[20:21], off offset:96
	global_load_dwordx4 v[116:119], v[18:19], off
	v_mov_b64_e32 v[18:19], s[6:7]
	v_mad_i64_i32 v[20:21], s[0:1], v23, s55, v[18:19]
	v_lshl_add_u64 v[20:21], v[20:21], 0, v[130:131]
	v_mad_i64_i32 v[18:19], s[0:1], v25, s55, v[18:19]
	v_lshl_add_u64 v[18:19], v[18:19], 0, v[130:131]
	global_load_dwordx4 v[120:123], v[20:21], off offset:128
	global_load_dwordx4 v[124:127], v[18:19], off offset:128
	v_lshlrev_b32_e32 v18, 1, v22
	v_lshrrev_b32_e32 v19, 1, v22
	s_movk_i32 s33, 0x90
	v_and_b32_e32 v18, 8, v18
	v_and_b32_e32 v19, 4, v19
	v_and_b32_e32 v20, 19, v22
	v_mul_lo_u32 v144, v128, s33
	v_lshlrev_b32_e32 v146, 4, v24
	v_or3_b32 v18, v18, v20, v19
	v_add3_u32 v19, 0, v144, v146
	v_mul_lo_u32 v147, v23, s33
	v_and_b32_e32 v142, 31, v22
	s_andn2_b32 s12, s12, 31
	v_mul_i32_i24_e32 v143, -8, v26
	s_lshl_b32 s35, s92, 8
	v_mul_u32_u24_e32 v148, 0x90, v18
	v_mov_b32_e32 v18, v3
	s_add_i32 s0, s12, s48
	v_mad_i64_i32 v[134:135], s[50:51], v23, s55, 0
	v_mad_i64_i32 v[136:137], s[50:51], v25, s55, 0
	v_lshl_add_u64 v[138:139], s[26:27], 0, v[16:17]
	v_mov_b32_e32 v16, v3
	v_mov_b32_e32 v17, v3
	v_readfirstlane_b32 s1, v145
	s_mov_b32 s31, 1
	s_or_b32 s13, s0, 31
	v_mul_u32_u24_e32 v129, 0x90, v142
	v_mov_b32_e32 v131, 0xf149f2ca
	v_mov_b32_e32 v141, 0
	s_movk_i32 s84, 0x80
	s_waitcnt vmcnt(0)
	ds_write_b128 v19, v[4:7]
	v_add3_u32 v4, 0, v130, v147
	ds_write_b128 v4, v[8:11] offset:9216
	ds_write_b128 v4, v[12:15] offset:18432
	v_add3_u32 v4, v143, s12, v142
	v_subrev_u32_e32 v4, s35, v4
	v_mov_b32_e32 v19, v3
	v_add_u32_e32 v149, 0x6e9, v4
	v_mov_b32_e32 v4, v3
	v_mov_b32_e32 v5, v3
	v_mov_b32_e32 v6, v3
	v_mov_b32_e32 v7, v3
	v_mov_b32_e32 v8, v3
	v_mov_b32_e32 v9, v3
	v_mov_b32_e32 v10, v3
	v_mov_b32_e32 v11, v3
	v_mov_b32_e32 v12, v3
	v_mov_b32_e32 v13, v3
	v_mov_b32_e32 v14, v3
	v_mov_b32_e32 v15, v3
	v_mov_b64_e32 v[34:35], v[18:19]
	v_mov_b64_e32 v[50:51], v[18:19]
	v_mov_b64_e32 v[66:67], v[18:19]
	v_mov_b64_e32 v[32:33], v[16:17]
	v_mov_b64_e32 v[30:31], v[14:15]
	v_mov_b64_e32 v[28:29], v[12:13]
	v_mov_b64_e32 v[26:27], v[10:11]
	v_mov_b64_e32 v[24:25], v[8:9]
	v_mov_b64_e32 v[22:23], v[6:7]
	v_mov_b64_e32 v[20:21], v[4:5]
	v_mov_b64_e32 v[48:49], v[16:17]
	v_mov_b64_e32 v[46:47], v[14:15]
	v_mov_b64_e32 v[44:45], v[12:13]
	v_mov_b64_e32 v[42:43], v[10:11]
	v_mov_b64_e32 v[40:41], v[8:9]
	v_mov_b64_e32 v[38:39], v[6:7]
	v_mov_b64_e32 v[36:37], v[4:5]
	v_mov_b64_e32 v[64:65], v[16:17]
	v_mov_b64_e32 v[62:63], v[14:15]
	v_mov_b64_e32 v[60:61], v[12:13]
	v_mov_b64_e32 v[58:59], v[10:11]
	v_mov_b64_e32 v[56:57], v[8:9]
	v_mov_b64_e32 v[54:55], v[6:7]
	v_mov_b64_e32 v[52:53], v[4:5]
	s_waitcnt lgkmcnt(0)
	s_barrier

.LBB6_1290:
	s_lshl_b32 s4, s37, 8
	s_lshl_b32 s0, s36, 11
	v_readlane_b32 s2, v254, 13
	s_add_i32 s1, s4, 0x100
	s_add_i32 s24, s4, s0
	s_mov_b32 s25, s85
	v_readlane_b32 s3, v254, 14
	s_lshr_b32 s34, s1, 6
	s_lshl_b64 s[0:1], s[24:25], 10
	s_add_u32 s0, s2, s0
	s_addc_u32 s1, s3, s1
	s_lshl_b32 s84, s74, 1
	s_add_u32 s28, s0, s84
	s_addc_u32 s29, s1, 0
	s_lshl_b32 s0, s36, 21
	s_add_u32 s0, s2, s0
	s_addc_u32 s1, s3, 0
	s_add_u32 s0, s0, s84
	s_addc_u32 s1, s1, 0
	v_mov_b32_e32 v183, v0
	s_add_u32 s26, s0, 0xc200000
	v_mov_b32_e32 v32, v0
	s_addc_u32 s27, s1, 0
	s_add_u32 s0, s2, s80
	v_ashrrev_i32_e32 v2, 31, v32
	v_lshrrev_b32_e32 v2, 28, v2
	s_addc_u32 s1, s3, 0
	s_lshl_b32 s5, s36, 12
	v_add_u32_e32 v2, v32, v2
	s_add_u32 s0, s0, s5
	v_ashrrev_i32_e32 v33, 4, v2
	v_and_b32_e32 v2, -16, v2
	s_addc_u32 s1, s1, 0
	v_sub_u32_e32 v34, v32, v2
	v_add_u32_e32 v2, 0x200, v32
	s_add_u32 s6, s0, 0xea40000
	v_readfirstlane_b32 s0, v32
	v_ashrrev_i32_e32 v4, 31, v2
	s_addc_u32 s7, s1, 0
	s_ashr_i32 s12, s0, 6
	v_lshrrev_b32_e32 v4, 28, v4
	s_lshl_b32 s13, s12, 5
	v_add_u32_e32 v4, v2, v4
	v_lshlrev_b32_e32 v6, 3, v34
	s_add_i32 s25, s13, s4
	v_ashrrev_i32_e32 v35, 4, v4
	v_and_b32_e32 v4, -16, v4
	s_or_b32 s0, s4, 0xc0
	v_ashrrev_i32_e32 v7, 31, v6
	s_mov_b32 s5, s85
	s_or_b32 s35, s25, 31
	v_sub_u32_e32 v36, v2, v4
	v_add_u32_e32 v4, s0, v33
	v_lshlrev_b64 v[20:21], 1, v[6:7]
	v_add_u32_e32 v6, s0, v35
	s_lshl_b64 s[0:1], s[4:5], 1
	v_and_b32_e32 v39, 31, v32
	s_add_u32 s0, s6, s0
	v_or_b32_e32 v28, s13, v39
	v_ashrrev_i32_e32 v37, 3, v32
	s_addc_u32 s1, s7, s1
	v_ashrrev_i32_e32 v29, 31, v28
	v_mov_b64_e32 v[16:17], s[0:1]
	v_lshlrev_b32_e32 v2, 4, v32
	v_add_u32_e32 v38, 64, v37
	v_bfe_u32 v40, v32, 5, 1
	v_lshlrev_b64 v[28:29], 10, v[28:29]
	v_ashrrev_i32_e32 v5, 31, v4
	v_ashrrev_i32_e32 v7, 31, v6
	v_lshlrev_b32_e32 v8, 3, v36
	v_mad_i64_i32 v[12:13], s[0:1], v37, s55, v[16:17]
	v_and_b32_e32 v184, 0x70, v2
	v_mad_i64_i32 v[16:17], s[0:1], v38, s55, v[16:17]
	v_lshl_add_u64 v[28:29], s[28:29], 0, v[28:29]
	v_lshlrev_b32_e32 v2, 4, v40
	v_lshlrev_b64 v[4:5], 10, v[4:5]
	v_lshlrev_b64 v[6:7], 10, v[6:7]
	v_ashrrev_i32_e32 v9, 31, v8
	v_lshl_add_u64 v[28:29], v[28:29], 0, v[2:3]
	s_mov_b64 s[0:1], 0xba00000
	v_lshl_add_u64 v[4:5], s[26:27], 0, v[4:5]
	v_lshl_add_u64 v[6:7], s[26:27], 0, v[6:7]
	v_lshlrev_b64 v[22:23], 1, v[8:9]
	v_mov_b32_e32 v185, v3
	v_lshl_add_u64 v[30:31], v[28:29], 0, s[0:1]
	s_mov_b32 s0, 0xba00000
	v_lshl_add_u64 v[4:5], v[4:5], 0, v[20:21]
	v_lshl_add_u64 v[8:9], v[6:7], 0, v[22:23]
	v_lshl_add_u64 v[24:25], v[12:13], 0, v[184:185]
	v_lshl_add_u64 v[26:27], v[16:17], 0, v[184:185]
	v_add_co_u32_e32 v28, vcc, s0, v28
	s_or_b32 s0, s4, 0x80
	global_load_dwordx4 v[4:7], v[4:5], off
	s_nop 0
	global_load_dwordx4 v[8:11], v[8:9], off
	v_addc_co_u32_e32 v29, vcc, 0, v29, vcc
	global_load_dwordx4 v[12:15], v[24:25], off offset:384
	global_load_dwordx4 v[16:19], v[26:27], off offset:384
	global_load_dwordx4 v[132:135], v[30:31], off offset:32
	global_load_dwordx4 v[136:139], v[30:31], off offset:64
	global_load_dwordx4 v[140:143], v[30:31], off offset:96
	global_load_dwordx4 v[144:147], v[30:31], off offset:128
	global_load_dwordx4 v[148:151], v[30:31], off offset:160
	global_load_dwordx4 v[152:155], v[30:31], off offset:192
	global_load_dwordx4 v[156:159], v[28:29], off
	global_load_dwordx4 v[160:163], v[30:31], off offset:224
	v_add_u32_e32 v28, s0, v33
	v_ashrrev_i32_e32 v29, 31, v28
	v_add_u32_e32 v30, s0, v35
	v_lshlrev_b64 v[28:29], 10, v[28:29]
	v_ashrrev_i32_e32 v31, 31, v30
	v_lshl_add_u64 v[28:29], s[26:27], 0, v[28:29]
	v_lshlrev_b64 v[30:31], 10, v[30:31]
	v_lshl_add_u64 v[28:29], v[28:29], 0, v[20:21]
	v_lshl_add_u64 v[30:31], s[26:27], 0, v[30:31]
	v_lshl_add_u64 v[30:31], v[30:31], 0, v[22:23]
	global_load_dwordx4 v[164:167], v[28:29], off
	global_load_dwordx4 v[168:171], v[30:31], off
	global_load_dwordx4 v[172:175], v[24:25], off offset:256
	global_load_dwordx4 v[176:179], v[26:27], off offset:256
	v_lshlrev_b32_e32 v25, 1, v32
	v_lshrrev_b32_e32 v26, 1, v32
	v_and_b32_e32 v25, 8, v25
	v_and_b32_e32 v26, 4, v26
	v_and_b32_e32 v28, 19, v32
	v_mul_lo_u32 v196, v33, s52
	v_lshlrev_b32_e32 v197, 4, v34
	v_or3_b32 v25, v28, v25, v26
	v_add3_u32 v26, 0, v196, v197
	v_mul_lo_u32 v198, v35, s52
	v_lshlrev_b32_e32 v199, 4, v36
	v_mad_i64_i32 v[186:187], s[0:1], v37, s55, 0
	v_mad_i64_i32 v[188:189], s[0:1], v38, s55, 0
	v_mul_lo_u32 v200, v37, s41
	s_add_i32 s1, s13, 0xffffff09
	v_lshlrev_b32_e32 v27, 3, v40
	s_lshl_b32 s0, s12, 2
	s_add_i32 s49, s0, 0
	s_lshl_b32 s0, s92, 8
	v_and_b32_e32 v24, 63, v32
	v_lshl_add_u64 v[192:193], s[26:27], 0, v[20:21]
	v_mov_b32_e32 v20, v3
	v_mov_b32_e32 v21, v3
	v_mov_b32_e32 v34, v3
	v_cmp_eq_u32_e64 s[4:5], 0, v24
	v_lshl_add_u64 v[190:191], s[6:7], 0, v[184:185]
	v_mul_u32_u24_e32 v185, 0x110, v25
	v_cmp_gt_u32_e64 s[6:7], 32, v24
	v_mul_u32_u24_e32 v201, 0x90, v39
	v_lshl_add_u64 v[194:195], s[26:27], 0, v[22:23]
	v_mov_b32_e32 v22, v3
	v_mov_b32_e32 v23, v3
	v_mov_b32_e32 v24, v3
	v_mov_b32_e32 v25, v3
	v_mov_b32_e32 v28, v3
	v_mov_b32_e32 v29, v3
	v_mov_b32_e32 v30, v3
	v_mov_b32_e32 v31, v3
	v_mov_b32_e32 v32, v3
	v_readfirstlane_b32 s47, v183
	s_mov_b32 s48, 0
	s_add_i32 s49, s49, 0x12000
	s_sub_i32 s50, 0, s0
	v_mov_b32_e32 v206, 0
	s_mov_b64 s[26:27], 0
	s_waitcnt vmcnt(0)
	ds_write_b128 v26, v[4:7]
	v_add3_u32 v4, 0, v198, v199
	ds_write_b128 v4, v[8:11]
	v_add3_u32 v4, 0, v184, v200
	ds_write_b128 v4, v[12:15] offset:17408
	ds_write_b128 v4, v[16:19] offset:26624
	v_add_u32_e32 v4, s1, v39
	v_sub_u32_e32 v205, v4, v27
	v_sub_u32_e32 v4, v27, v39
	v_subrev_u32_e32 v202, s13, v4
	v_subrev_u32_e32 v4, s0, v35
	v_add_u32_e32 v203, 0x740, v4
	v_subrev_u32_e32 v4, s0, v33
	v_mov_b32_e32 v35, v3
	v_add_u32_e32 v204, 0x740, v4
	v_mov_b32_e32 v26, v3
	v_mov_b32_e32 v27, v3
	v_mov_b32_e32 v33, v3
	v_mov_b64_e32 v[66:67], v[34:35]
	v_mov_b64_e32 v[50:51], v[34:35]
	v_mov_b64_e32 v[4:5], v[20:21]
	v_mov_b64_e32 v[64:65], v[32:33]
	v_mov_b64_e32 v[62:63], v[30:31]
	v_mov_b64_e32 v[60:61], v[28:29]
	v_mov_b64_e32 v[58:59], v[26:27]
	v_mov_b64_e32 v[56:57], v[24:25]
	v_mov_b64_e32 v[54:55], v[22:23]
	v_mov_b64_e32 v[52:53], v[20:21]
	v_mov_b64_e32 v[48:49], v[32:33]
	v_mov_b64_e32 v[46:47], v[30:31]
	v_mov_b64_e32 v[44:45], v[28:29]
	v_mov_b64_e32 v[42:43], v[26:27]
	v_mov_b64_e32 v[40:41], v[24:25]
	v_mov_b64_e32 v[38:39], v[22:23]
	v_mov_b64_e32 v[36:37], v[20:21]
	v_mov_b64_e32 v[6:7], v[22:23]
	v_mov_b64_e32 v[8:9], v[24:25]
	v_mov_b64_e32 v[10:11], v[26:27]
	v_mov_b64_e32 v[12:13], v[28:29]
	v_mov_b64_e32 v[14:15], v[30:31]
	v_mov_b64_e32 v[16:17], v[32:33]
	v_mov_b64_e32 v[18:19], v[34:35]
	s_mov_b32 s0, 0
	s_waitcnt lgkmcnt(0)
	s_barrier
	s_cmp_eq_u32 s34, s0
	s_cbranch_scc0 .LBB6_1292
